# grid barrier: each workgroup's L1 invalidate (acquire) is issued at arrival, before the spin (spin loads are sc1 = L1-bypassing, no other loads in between), so it overlaps the wait instead of followin
# speedup vs baseline: 1.0044x; 1.0044x over previous
.Lpf_skip_0:
	buffer_inv sc1
	s_waitcnt lgkmcnt(0)
	v_mov_b32_e32 v1, 0x2000
	global_load_dword v1, v1, s[8:9] offset:1024 sc1
	s_add_u32 s16, s8, 0x2400
	s_addc_u32 s17, s9, 0
	s_waitcnt vmcnt(0)
	v_cmp_eq_u32_e32 vcc, v1, v2
	s_and_saveexec_b64 s[12:13], vcc
	s_cbranch_execz .LBB0_86
	v_readlane_b32 s0, v253, 4
	v_readlane_b32 s1, v253, 5
	s_add_u32 s14, s0, 0x4200
	s_addc_u32 s15, s1, 0
	s_mov_b32 s0, 1
	s_mov_b64 s[18:19], 0
	v_mov_b32_e32 v1, 0
	s_branch .LBB0_77

.LBB0_86:
	s_or_b64 exec, exec, s[12:13]
	s_waitcnt vmcnt(0)
	s_waitcnt vmcnt(0)
.LBB0_87:
	s_andn2_saveexec_b64 s[0:1], s[10:11]
	s_cbranch_execz .LBB0_107
	s_mov_b64 s[10:11], exec
	buffer_wbl2 sc1
	buffer_inv sc1
	s_waitcnt lgkmcnt(0)
	s_waitcnt vmcnt(0)
	v_mbcnt_lo_u32_b32 v2, s10, 0
	v_mbcnt_hi_u32_b32 v2, s11, v2
	v_cmp_eq_u32_e32 vcc, 0, v2
	s_and_saveexec_b64 s[12:13], vcc
	s_cbranch_execz .LBB0_90
	s_bcnt1_i32_b64 s0, s[10:11]
	v_mov_b32_e32 v4, s0
	v_readlane_b32 s0, v253, 4
	v_mov_b32_e32 v3, 0x7000
	v_readlane_b32 s1, v253, 5
	s_nop 4
	global_atomic_add v3, v3, v4, s[0:1] offset:1024 sc0

.Lpf_skip_17:
	buffer_inv sc1
	s_waitcnt lgkmcnt(0)
	v_mov_b32_e32 v1, 0x2000
	global_load_dword v1, v1, s[4:5] offset:1024 sc1
	s_add_u32 s14, s4, 0x2400
	s_addc_u32 s15, s5, 0
	s_waitcnt vmcnt(0)
	v_cmp_eq_u32_e32 vcc, v1, v2
	s_and_saveexec_b64 s[10:11], vcc
	s_cbranch_execz .LBB0_2271
	v_readlane_b32 s0, v253, 4
	v_readlane_b32 s1, v253, 5
	s_add_u32 s12, s0, 0x4200
	s_addc_u32 s13, s1, 0
	s_mov_b32 s0, 1
	s_mov_b64 s[16:17], 0
	v_mov_b32_e32 v1, 0
	s_branch .LBB0_2262

.LBB0_2271:
	s_or_b64 exec, exec, s[10:11]
	s_waitcnt vmcnt(0)
	s_waitcnt vmcnt(0)
.LBB0_2272:
	s_andn2_saveexec_b64 s[0:1], s[8:9]
	s_cbranch_execz .LBB0_2292
	s_mov_b64 s[8:9], exec
	buffer_wbl2 sc1
	buffer_inv sc1
	s_waitcnt lgkmcnt(0)
	s_waitcnt vmcnt(0)
	v_mbcnt_lo_u32_b32 v2, s8, 0
	v_mbcnt_hi_u32_b32 v2, s9, v2
	v_cmp_eq_u32_e32 vcc, 0, v2
	s_and_saveexec_b64 s[10:11], vcc
	s_cbranch_execz .LBB0_2275
	s_bcnt1_i32_b64 s0, s[8:9]
	v_mov_b32_e32 v4, s0
	v_readlane_b32 s0, v253, 4
	v_mov_b32_e32 v3, 0x7000
	v_readlane_b32 s1, v253, 5
	s_nop 4
	global_atomic_add v3, v3, v4, s[0:1] offset:1024 sc0
